# speedup vs baseline: 1.0225x; 1.0225x over previous
_Z8moe_gemmILi2048ELi1024ELb0EEvPKDF16_S1_PKfPDF16_PfPKiS7_:
	s_load_dwordx2 s[14:15], s[0:1], 0x28
	s_load_dword s20, s[0:1], 0x38
	s_load_dwordx4 s[4:7], s[0:1], 0x0
	s_load_dwordx4 s[8:11], s[0:1], 0x10
	s_load_dwordx2 s[12:13], s[0:1], 0x20
	s_load_dwordx2 s[16:17], s[0:1], 0x30
	v_lshrrev_b32_e32 v1, 6, v0
	v_and_b32_e32 v2, 63, v0
	v_readfirstlane_b32 s58, v1
	s_waitcnt lgkmcnt(0)
	s_load_dword s24, s[14:15], 0x0
	s_load_dword s25, s[14:15], 0x80
	s_load_dword s26, s[14:15], 0x100
	s_load_dword s27, s[14:15], 0x180
	s_load_dword s28, s[14:15], 0x200
	s_load_dword s29, s[14:15], 0x280
	s_load_dword s30, s[14:15], 0x300
	s_load_dword s31, s[14:15], 0x380
	s_lshr_b32 s59, s58, 1
	s_and_b32 s60, s58, 1
	s_lshl_b32 s70, s58, 10
	s_movk_i32 s69, 0x1080
	v_and_b32_e32 v3, 15, v2
	v_lshrrev_b32_e32 v4, 4, v2
	v_lshrrev_b32_e32 v5, 3, v0
	v_bfe_u32 v8, v5, 1, 3
	v_bfe_u32 v9, v5, 4, 1
	v_xor_b32_e32 v8, v8, v9
	v_and_b32_e32 v9, 7, v0
	v_xor_b32_e32 v8, v8, v9
	v_lshlrev_b32_e32 v6, 4, v8
	v_bfe_u32 v8, v0, 4, 2
	v_bfe_u32 v9, v0, 7, 1
	v_lshl_or_b32 v8, v9, 2, v8
	v_lshlrev_b32_e32 v8, 1, v8
	v_and_b32_e32 v9, 15, v0
	v_xor_b32_e32 v8, v8, v9
	v_lshlrev_b32_e32 v8, 4, v8
	v_lshrrev_b32_e32 v9, 4, v0
	v_lshlrev_b32_e32 v9, 11, v9
	v_add_u32_e32 v7, v8, v9
	v_bfe_u32 v8, v2, 2, 2
	v_and_b32_e32 v9, 1, v4
	v_lshl_or_b32 v56, v9, 2, v8
	v_lshl_add_u32 v8, v4, 3, v8
	v_lshlrev_b32_e32 v8, 8, v8
	v_and_b32_e32 v9, 3, v2
	v_lshlrev_b32_e32 v9, 3, v9
	v_add_u32_e32 v8, v8, v9
	s_lshl_b32 s74, s60, 14
	s_add_u32 s74, s74, 0x5000
	v_add_u32_e32 v8, s74, v8
	v_xor_b32_e32 v9, 0, v56
	v_lshl_add_u32 v40, v9, 5, v8
	v_add_u32_e32 v48, 0xd000, v40
	v_xor_b32_e32 v9, 1, v56
	v_lshl_add_u32 v41, v9, 5, v8
	v_add_u32_e32 v49, 0xd000, v41
	v_xor_b32_e32 v9, 2, v56
	v_lshl_add_u32 v42, v9, 5, v8
	v_add_u32_e32 v50, 0xd000, v42
	v_xor_b32_e32 v9, 3, v56
	v_lshl_add_u32 v43, v9, 5, v8
	v_add_u32_e32 v51, 0xd000, v43
	v_xor_b32_e32 v9, 4, v56
	v_lshl_add_u32 v44, v9, 5, v8
	v_add_u32_e32 v52, 0xd000, v44
	v_xor_b32_e32 v9, 5, v56
	v_lshl_add_u32 v45, v9, 5, v8
	v_add_u32_e32 v53, 0xd000, v45
	v_xor_b32_e32 v9, 6, v56
	v_lshl_add_u32 v46, v9, 5, v8
	v_add_u32_e32 v54, 0xd000, v46
	v_xor_b32_e32 v9, 7, v56
	v_lshl_add_u32 v47, v9, 5, v8
	v_add_u32_e32 v55, 0xd000, v47
	s_waitcnt lgkmcnt(0)
	v_writelane_b32 v58, s24, 0
	v_writelane_b32 v58, s25, 1
	v_writelane_b32 v58, s26, 2
	v_writelane_b32 v58, s27, 3
	v_writelane_b32 v58, s28, 4
	v_writelane_b32 v58, s29, 5
	v_writelane_b32 v58, s30, 6
	v_writelane_b32 v58, s31, 7
	s_mov_b32 s22, 0xcccccccd
	v_add_u32_e32 v59, 0x9f, v58
	v_lshrrev_b32_e32 v59, 5, v59
	v_mul_hi_u32 v59, v59, s22
	v_lshrrev_b32_e32 v59, 2, v59
	v_add_u32_e32 v60, 15, v58
	v_lshrrev_b32_e32 v60, 4, v60
	v_add3_u32 v60, v60, v59, -1
	v_cvt_f32_i32_e32 v62, v59
	v_cvt_f32_i32_e32 v60, v60
	v_rcp_iflag_f32_e32 v62, v62
	v_add_f32_e32 v60, 0.5, v60
	v_cmp_eq_u32_e32 vcc, 0, v59
	v_mul_f32_e32 v61, v60, v62
	v_cvt_i32_f32_e32 v61, v61
	s_nop 1
	v_cndmask_b32_e32 v61, v61, v59, vcc
	s_nop 1
	v_readlane_b32 s32, v59, 0
	v_readlane_b32 s40, v61, 0
	v_readlane_b32 s33, v59, 1
	v_readlane_b32 s41, v61, 1
	v_readlane_b32 s34, v59, 2
	v_readlane_b32 s42, v61, 2
	v_readlane_b32 s35, v59, 3
	v_readlane_b32 s43, v61, 3
	v_readlane_b32 s36, v59, 4
	v_readlane_b32 s44, v61, 4
	v_readlane_b32 s37, v59, 5
	v_readlane_b32 s45, v61, 5
	v_readlane_b32 s38, v59, 6
	v_readlane_b32 s46, v61, 6
	v_readlane_b32 s39, v59, 7
	v_readlane_b32 s47, v61, 7
	s_add_i32 s21, s32, s33
	s_add_i32 s21, s21, s34
	s_add_i32 s21, s21, s35
	s_add_i32 s21, s21, s36
	s_add_i32 s21, s21, s37
	s_add_i32 s21, s21, s38
	s_add_i32 s21, s21, s39
	s_lshl_b32 s21, s21, 2
	s_and_b32 s22, s2, 7
	s_mul_i32 s23, s21, s22
	s_ashr_i32 s18, s23, 3
	s_add_i32 s23, s23, s21
	s_ashr_i32 s19, s23, 3
	s_lshr_b32 s22, s2, 3
	s_add_i32 s18, s18, s22
	s_lshr_b32 s20, s20, 3
	s_cmp_ge_i32 s18, s19
	s_cbranch_scc1 .Lg2_end
